# v5 plus 64-byte alignment of the eight GEMM K-loop heads
# speedup vs baseline: 1.0030x; 1.0030x over previous
.LBB0_631:
	s_ashr_i32 s25, s24, 31
	s_lshl_b64 s[28:29], s[24:25], 17
	s_add_u32 s28, s3, s28
	s_addc_u32 s29, s33, s29
	s_and_b64 s[34:35], s[30:31], exec
	s_cselect_b32 s5, s29, s41
	s_cselect_b32 s25, s28, s40
	s_ashr_i32 s27, s26, 31
	s_lshl_b64 s[34:35], s[26:27], 17
	s_add_u32 s34, s56, s34
	s_addc_u32 s35, s57, s35
	s_and_b64 s[42:43], s[30:31], exec
	v_mov_b32_e32 v2, 0
	s_cselect_b32 s27, s35, s39
	s_cselect_b32 s73, s34, s38
	s_mov_b64 s[46:47], 0
	s_mov_b64 s[42:43], -1
	s_mov_b64 s[44:45], 0
	v_mov_b32_e32 v3, v2
	v_mov_b32_e32 v4, v2
	v_mov_b32_e32 v5, v2
	v_mov_b32_e32 v6, v2
	v_mov_b32_e32 v7, v2
	v_mov_b32_e32 v8, v2
	v_mov_b32_e32 v9, v2
	v_mov_b32_e32 v18, v2
	v_mov_b32_e32 v19, v2
	v_mov_b32_e32 v20, v2
	v_mov_b32_e32 v21, v2
	v_mov_b32_e32 v22, v2
	v_mov_b32_e32 v23, v2
	v_mov_b32_e32 v24, v2
	v_mov_b32_e32 v25, v2
	v_mov_b32_e32 v34, v2
	v_mov_b32_e32 v35, v2
	v_mov_b32_e32 v36, v2
	v_mov_b32_e32 v37, v2
	v_mov_b32_e32 v38, v2
	v_mov_b32_e32 v39, v2
	v_mov_b32_e32 v40, v2
	v_mov_b32_e32 v41, v2
	v_mov_b32_e32 v50, v2
	v_mov_b32_e32 v51, v2
	v_mov_b32_e32 v52, v2
	v_mov_b32_e32 v53, v2
	v_mov_b32_e32 v54, v2
	v_mov_b32_e32 v55, v2
	v_mov_b32_e32 v56, v2
	v_mov_b32_e32 v57, v2
	v_mov_b32_e32 v10, v2
	v_mov_b32_e32 v11, v2
	v_mov_b32_e32 v12, v2
	v_mov_b32_e32 v13, v2
	v_mov_b32_e32 v14, v2
	v_mov_b32_e32 v15, v2
	v_mov_b32_e32 v16, v2
	v_mov_b32_e32 v17, v2
	v_mov_b32_e32 v26, v2
	v_mov_b32_e32 v27, v2
	v_mov_b32_e32 v28, v2
	v_mov_b32_e32 v29, v2
	v_mov_b32_e32 v30, v2
	v_mov_b32_e32 v31, v2
	v_mov_b32_e32 v32, v2
	v_mov_b32_e32 v33, v2
	v_mov_b32_e32 v42, v2
	v_mov_b32_e32 v43, v2
	v_mov_b32_e32 v44, v2
	v_mov_b32_e32 v45, v2
	v_mov_b32_e32 v46, v2
	v_mov_b32_e32 v47, v2
	v_mov_b32_e32 v48, v2
	v_mov_b32_e32 v49, v2
	v_mov_b32_e32 v58, v2
	v_mov_b32_e32 v59, v2
	v_mov_b32_e32 v60, v2
	v_mov_b32_e32 v61, v2
	v_mov_b32_e32 v62, v2
	v_mov_b32_e32 v63, v2
	v_mov_b32_e32 v64, v2
	v_mov_b32_e32 v65, v2
	v_mov_b32_e32 v66, v2
	v_mov_b32_e32 v67, v2
	v_mov_b32_e32 v68, v2
	v_mov_b32_e32 v69, v2
	v_mov_b32_e32 v70, v2
	v_mov_b32_e32 v71, v2
	v_mov_b32_e32 v72, v2
	v_mov_b32_e32 v73, v2
	v_mov_b32_e32 v82, v2
	v_mov_b32_e32 v83, v2
	v_mov_b32_e32 v84, v2
	v_mov_b32_e32 v85, v2
	v_mov_b32_e32 v86, v2
	v_mov_b32_e32 v87, v2
	v_mov_b32_e32 v88, v2
	v_mov_b32_e32 v89, v2
	v_mov_b32_e32 v98, v2
	v_mov_b32_e32 v99, v2
	v_mov_b32_e32 v100, v2
	v_mov_b32_e32 v101, v2
	v_mov_b32_e32 v102, v2
	v_mov_b32_e32 v103, v2
	v_mov_b32_e32 v104, v2
	v_mov_b32_e32 v105, v2
	v_mov_b32_e32 v114, v2
	v_mov_b32_e32 v115, v2
	v_mov_b32_e32 v116, v2
	v_mov_b32_e32 v117, v2
	v_mov_b32_e32 v118, v2
	v_mov_b32_e32 v119, v2
	v_mov_b32_e32 v120, v2
	v_mov_b32_e32 v121, v2
	v_mov_b32_e32 v74, v2
	v_mov_b32_e32 v75, v2
	v_mov_b32_e32 v76, v2
	v_mov_b32_e32 v77, v2
	v_mov_b32_e32 v78, v2
	v_mov_b32_e32 v79, v2
	v_mov_b32_e32 v80, v2
	v_mov_b32_e32 v81, v2
	v_mov_b32_e32 v90, v2
	v_mov_b32_e32 v91, v2
	v_mov_b32_e32 v92, v2
	v_mov_b32_e32 v93, v2
	v_mov_b32_e32 v94, v2
	v_mov_b32_e32 v95, v2
	v_mov_b32_e32 v96, v2
	v_mov_b32_e32 v97, v2
	v_mov_b32_e32 v106, v2
	v_mov_b32_e32 v107, v2
	v_mov_b32_e32 v108, v2
	v_mov_b32_e32 v109, v2
	v_mov_b32_e32 v110, v2
	v_mov_b32_e32 v111, v2
	v_mov_b32_e32 v112, v2
	v_mov_b32_e32 v113, v2
	v_mov_b32_e32 v122, v2
	v_mov_b32_e32 v123, v2
	v_mov_b32_e32 v124, v2
	v_mov_b32_e32 v125, v2
	v_mov_b32_e32 v126, v2
	v_mov_b32_e32 v127, v2
	v_mov_b32_e32 v128, v2
	v_mov_b32_e32 v129, v2
	.p2align 6

.LBB0_740:
	s_ashr_i32 s15, s14, 31
	s_lshl_b64 s[16:17], s[14:15], 18
	s_add_u32 s16, s27, s16
	s_addc_u32 s17, s33, s17
	s_and_b64 s[18:19], s[38:39], exec
	s_cselect_b32 s15, s17, s21
	s_cselect_b32 s53, s16, s20
	s_ashr_i32 s13, s12, 31
	s_lshl_b64 s[18:19], s[12:13], 18
	s_add_u32 s18, s34, s18
	s_addc_u32 s19, s40, s19
	s_and_b64 s[24:25], s[38:39], exec
	s_cselect_b32 s13, s19, s23
	s_cselect_b32 s54, s18, s22
	s_add_u32 s20, s20, 0x20080
	s_addc_u32 s21, s21, 0
	s_add_u32 s55, s22, 0x100
	s_waitcnt vmcnt(0)
	v_mov_b32_e32 v32, 0
	s_addc_u32 s56, s23, 0
	s_mov_b32 s57, -2
	v_mov_b32_e32 v33, v32
	v_mov_b32_e32 v34, v32
	v_mov_b32_e32 v35, v32
	v_mov_b32_e32 v36, v32
	v_mov_b32_e32 v37, v32
	v_mov_b32_e32 v38, v32
	v_mov_b32_e32 v39, v32
	v_mov_b32_e32 v48, v32
	v_mov_b32_e32 v49, v32
	v_mov_b32_e32 v50, v32
	v_mov_b32_e32 v51, v32
	v_mov_b32_e32 v52, v32
	v_mov_b32_e32 v53, v32
	v_mov_b32_e32 v54, v32
	v_mov_b32_e32 v55, v32
	v_mov_b32_e32 v66, v32
	v_mov_b32_e32 v67, v32
	v_mov_b32_e32 v68, v32
	v_mov_b32_e32 v69, v32
	v_mov_b32_e32 v70, v32
	v_mov_b32_e32 v71, v32
	v_mov_b32_e32 v72, v32
	v_mov_b32_e32 v73, v32
	v_mov_b32_e32 v82, v32
	v_mov_b32_e32 v83, v32
	v_mov_b32_e32 v84, v32
	v_mov_b32_e32 v85, v32
	v_mov_b32_e32 v86, v32
	v_mov_b32_e32 v87, v32
	v_mov_b32_e32 v88, v32
	v_mov_b32_e32 v89, v32
	v_mov_b32_e32 v40, v32
	v_mov_b32_e32 v41, v32
	v_mov_b32_e32 v42, v32
	v_mov_b32_e32 v43, v32
	v_mov_b32_e32 v44, v32
	v_mov_b32_e32 v45, v32
	v_mov_b32_e32 v46, v32
	v_mov_b32_e32 v47, v32
	v_mov_b32_e32 v56, v32
	v_mov_b32_e32 v57, v32
	v_mov_b32_e32 v58, v32
	v_mov_b32_e32 v59, v32
	v_mov_b32_e32 v60, v32
	v_mov_b32_e32 v61, v32
	v_mov_b32_e32 v62, v32
	v_mov_b32_e32 v63, v32
	v_mov_b32_e32 v74, v32
	v_mov_b32_e32 v75, v32
	v_mov_b32_e32 v76, v32
	v_mov_b32_e32 v77, v32
	v_mov_b32_e32 v78, v32
	v_mov_b32_e32 v79, v32
	v_mov_b32_e32 v80, v32
	v_mov_b32_e32 v81, v32
	v_mov_b32_e32 v90, v32
	v_mov_b32_e32 v91, v32
	v_mov_b32_e32 v92, v32
	v_mov_b32_e32 v93, v32
	v_mov_b32_e32 v94, v32
	v_mov_b32_e32 v95, v32
	v_mov_b32_e32 v96, v32
	v_mov_b32_e32 v97, v32
	v_mov_b32_e32 v98, v32
	v_mov_b32_e32 v99, v32
	v_mov_b32_e32 v100, v32
	v_mov_b32_e32 v101, v32
	v_mov_b32_e32 v102, v32
	v_mov_b32_e32 v103, v32
	v_mov_b32_e32 v104, v32
	v_mov_b32_e32 v105, v32
	v_mov_b32_e32 v114, v32
	v_mov_b32_e32 v115, v32
	v_mov_b32_e32 v116, v32
	v_mov_b32_e32 v117, v32
	v_mov_b32_e32 v118, v32
	v_mov_b32_e32 v119, v32
	v_mov_b32_e32 v120, v32
	v_mov_b32_e32 v121, v32
	v_mov_b32_e32 v130, v32
	v_mov_b32_e32 v131, v32
	v_mov_b32_e32 v132, v32
	v_mov_b32_e32 v133, v32
	v_mov_b32_e32 v134, v32
	v_mov_b32_e32 v135, v32
	v_mov_b32_e32 v136, v32
	v_mov_b32_e32 v137, v32
	v_mov_b32_e32 v146, v32
	v_mov_b32_e32 v147, v32
	v_mov_b32_e32 v148, v32
	v_mov_b32_e32 v149, v32
	v_mov_b32_e32 v150, v32
	v_mov_b32_e32 v151, v32
	v_mov_b32_e32 v152, v32
	v_mov_b32_e32 v153, v32
	v_mov_b32_e32 v106, v32
	v_mov_b32_e32 v107, v32
	v_mov_b32_e32 v108, v32
	v_mov_b32_e32 v109, v32
	v_mov_b32_e32 v110, v32
	v_mov_b32_e32 v111, v32
	v_mov_b32_e32 v112, v32
	v_mov_b32_e32 v113, v32
	v_mov_b32_e32 v122, v32
	v_mov_b32_e32 v123, v32
	v_mov_b32_e32 v124, v32
	v_mov_b32_e32 v125, v32
	v_mov_b32_e32 v126, v32
	v_mov_b32_e32 v127, v32
	v_mov_b32_e32 v128, v32
	v_mov_b32_e32 v129, v32
	v_mov_b32_e32 v138, v32
	v_mov_b32_e32 v139, v32
	v_mov_b32_e32 v140, v32
	v_mov_b32_e32 v141, v32
	v_mov_b32_e32 v142, v32
	v_mov_b32_e32 v143, v32
	v_mov_b32_e32 v144, v32
	v_mov_b32_e32 v145, v32
	v_mov_b32_e32 v154, v32
	v_mov_b32_e32 v155, v32
	v_mov_b32_e32 v156, v32
	v_mov_b32_e32 v157, v32
	v_mov_b32_e32 v158, v32
	v_mov_b32_e32 v159, v32
	v_mov_b32_e32 v160, v32
	v_mov_b32_e32 v161, v32
	.p2align 6

.LBB0_756:
	s_ashr_i32 s13, s12, 31
	s_lshl_b64 s[14:15], s[12:13], 19
	s_add_u32 s14, s25, s14
	s_addc_u32 s15, s27, s15
	s_and_b64 s[16:17], s[38:39], exec
	s_cselect_b32 s13, s15, s19
	s_cselect_b32 s51, s14, s18
	s_ashr_i32 s11, s10, 31
	s_lshl_b64 s[16:17], s[10:11], 19
	s_add_u32 s16, s33, s16
	s_addc_u32 s17, s34, s17
	s_and_b64 s[22:23], s[38:39], exec
	s_cselect_b32 s11, s17, s21
	s_cselect_b32 s52, s16, s20
	s_add_u32 s18, s18, 0x40080
	s_addc_u32 s19, s19, 0
	s_add_u32 s53, s20, 0x100
	v_mov_b32_e32 v0, 0
	s_addc_u32 s54, s21, 0
	s_mov_b32 s55, -2
	v_mov_b32_e32 v1, v0
	v_mov_b32_e32 v2, v0
	v_mov_b32_e32 v3, v0
	v_mov_b32_e32 v4, v0
	v_mov_b32_e32 v5, v0
	v_mov_b32_e32 v6, v0
	v_mov_b32_e32 v7, v0
	v_mov_b32_e32 v16, v0
	v_mov_b32_e32 v17, v0
	v_mov_b32_e32 v18, v0
	v_mov_b32_e32 v19, v0
	v_mov_b32_e32 v20, v0
	v_mov_b32_e32 v21, v0
	v_mov_b32_e32 v22, v0
	v_mov_b32_e32 v23, v0
	s_waitcnt vmcnt(0)
	v_mov_b32_e32 v32, v0
	v_mov_b32_e32 v33, v0
	v_mov_b32_e32 v34, v0
	v_mov_b32_e32 v35, v0
	v_mov_b32_e32 v36, v0
	v_mov_b32_e32 v37, v0
	v_mov_b32_e32 v38, v0
	v_mov_b32_e32 v39, v0
	v_mov_b32_e32 v48, v0
	v_mov_b32_e32 v49, v0
	v_mov_b32_e32 v50, v0
	v_mov_b32_e32 v51, v0
	v_mov_b32_e32 v52, v0
	v_mov_b32_e32 v53, v0
	v_mov_b32_e32 v54, v0
	v_mov_b32_e32 v55, v0
	v_mov_b32_e32 v8, v0
	v_mov_b32_e32 v9, v0
	v_mov_b32_e32 v10, v0
	v_mov_b32_e32 v11, v0
	v_mov_b32_e32 v12, v0
	v_mov_b32_e32 v13, v0
	v_mov_b32_e32 v14, v0
	v_mov_b32_e32 v15, v0
	v_mov_b32_e32 v24, v0
	v_mov_b32_e32 v25, v0
	v_mov_b32_e32 v26, v0
	v_mov_b32_e32 v27, v0
	v_mov_b32_e32 v28, v0
	v_mov_b32_e32 v29, v0
	v_mov_b32_e32 v30, v0
	v_mov_b32_e32 v31, v0
	v_mov_b32_e32 v40, v0
	v_mov_b32_e32 v41, v0
	v_mov_b32_e32 v42, v0
	v_mov_b32_e32 v43, v0
	v_mov_b32_e32 v44, v0
	v_mov_b32_e32 v45, v0
	v_mov_b32_e32 v46, v0
	v_mov_b32_e32 v47, v0
	v_mov_b32_e32 v56, v0
	v_mov_b32_e32 v57, v0
	v_mov_b32_e32 v58, v0
	v_mov_b32_e32 v59, v0
	v_mov_b32_e32 v60, v0
	v_mov_b32_e32 v61, v0
	v_mov_b32_e32 v62, v0
	v_mov_b32_e32 v63, v0
	v_mov_b32_e32 v66, v0
	v_mov_b32_e32 v67, v0
	v_mov_b32_e32 v68, v0
	v_mov_b32_e32 v69, v0
	v_mov_b32_e32 v70, v0
	v_mov_b32_e32 v71, v0
	v_mov_b32_e32 v72, v0
	v_mov_b32_e32 v73, v0
	v_mov_b32_e32 v82, v0
	v_mov_b32_e32 v83, v0
	v_mov_b32_e32 v84, v0
	v_mov_b32_e32 v85, v0
	v_mov_b32_e32 v86, v0
	v_mov_b32_e32 v87, v0
	v_mov_b32_e32 v88, v0
	v_mov_b32_e32 v89, v0
	v_mov_b32_e32 v98, v0
	v_mov_b32_e32 v99, v0
	v_mov_b32_e32 v100, v0
	v_mov_b32_e32 v101, v0
	v_mov_b32_e32 v102, v0
	v_mov_b32_e32 v103, v0
	v_mov_b32_e32 v104, v0
	v_mov_b32_e32 v105, v0
	v_mov_b32_e32 v114, v0
	v_mov_b32_e32 v115, v0
	v_mov_b32_e32 v116, v0
	v_mov_b32_e32 v117, v0
	v_mov_b32_e32 v118, v0
	v_mov_b32_e32 v119, v0
	v_mov_b32_e32 v120, v0
	v_mov_b32_e32 v121, v0
	v_mov_b32_e32 v74, v0
	v_mov_b32_e32 v75, v0
	v_mov_b32_e32 v76, v0
	v_mov_b32_e32 v77, v0
	v_mov_b32_e32 v78, v0
	v_mov_b32_e32 v79, v0
	v_mov_b32_e32 v80, v0
	v_mov_b32_e32 v81, v0
	v_mov_b32_e32 v90, v0
	v_mov_b32_e32 v91, v0
	v_mov_b32_e32 v92, v0
	v_mov_b32_e32 v93, v0
	v_mov_b32_e32 v94, v0
	v_mov_b32_e32 v95, v0
	v_mov_b32_e32 v96, v0
	v_mov_b32_e32 v97, v0
	v_mov_b32_e32 v106, v0
	v_mov_b32_e32 v107, v0
	v_mov_b32_e32 v108, v0
	v_mov_b32_e32 v109, v0
	v_mov_b32_e32 v110, v0
	v_mov_b32_e32 v111, v0
	v_mov_b32_e32 v112, v0
	v_mov_b32_e32 v113, v0
	v_mov_b32_e32 v122, v0
	v_mov_b32_e32 v123, v0
	v_mov_b32_e32 v124, v0
	v_mov_b32_e32 v125, v0
	v_mov_b32_e32 v126, v0
	v_mov_b32_e32 v127, v0
	v_mov_b32_e32 v128, v0
	v_mov_b32_e32 v129, v0
	.p2align 6

.LBB0_1717:
	s_ashr_i32 s15, s14, 31
	s_lshl_b64 s[16:17], s[14:15], 17
	s_add_u32 s16, s26, s16
	s_addc_u32 s17, s27, s17
	s_and_b64 s[18:19], s[40:41], exec
	s_cselect_b32 s15, s17, s23
	s_cselect_b32 s64, s16, s22
	s_ashr_i32 s13, s12, 31
	s_lshl_b64 s[18:19], s[12:13], 17
	s_add_u32 s18, s33, s18
	s_addc_u32 s19, s34, s19
	s_and_b64 s[24:25], s[40:41], exec
	s_cselect_b32 s13, s19, s21
	s_cselect_b32 s65, s18, s20
	s_mov_b64 s[44:45], 0
	s_mov_b64 s[24:25], -1
	s_mov_b64 s[42:43], 0
	v_mov_b32_e32 v32, v40
	v_mov_b32_e32 v33, v41
	v_mov_b32_e32 v34, v46
	v_mov_b32_e32 v35, v47
	v_mov_b32_e32 v36, v42
	v_mov_b32_e32 v37, v43
	v_mov_b32_e32 v38, v44
	v_mov_b32_e32 v39, v45
	v_mov_b32_e32 v48, v56
	v_mov_b32_e32 v49, v57
	v_mov_b32_e32 v50, v62
	v_mov_b32_e32 v51, v63
	v_mov_b32_e32 v52, v58
	v_mov_b32_e32 v53, v59
	v_mov_b32_e32 v54, v60
	v_mov_b32_e32 v55, v61
	v_mov_b32_e32 v66, v74
	v_mov_b32_e32 v67, v75
	v_mov_b32_e32 v68, v80
	v_mov_b32_e32 v69, v81
	v_mov_b32_e32 v70, v76
	v_mov_b32_e32 v71, v77
	v_mov_b32_e32 v72, v78
	v_mov_b32_e32 v73, v79
	v_mov_b32_e32 v82, v90
	v_mov_b32_e32 v83, v91
	v_mov_b32_e32 v84, v96
	v_mov_b32_e32 v85, v97
	v_mov_b32_e32 v86, v92
	v_mov_b32_e32 v87, v93
	v_mov_b32_e32 v88, v94
	v_mov_b32_e32 v89, v95
	v_mov_b32_e32 v40, v146
	v_mov_b32_e32 v41, v147
	v_mov_b32_e32 v42, v152
	v_mov_b32_e32 v43, v153
	v_mov_b32_e32 v44, v148
	v_mov_b32_e32 v45, v149
	v_mov_b32_e32 v46, v150
	v_mov_b32_e32 v47, v151
	v_mov_b32_e32 v56, v130
	v_mov_b32_e32 v57, v131
	v_mov_b32_e32 v58, v136
	v_mov_b32_e32 v59, v137
	v_mov_b32_e32 v60, v132
	v_mov_b32_e32 v61, v133
	v_mov_b32_e32 v62, v134
	v_mov_b32_e32 v63, v135
	v_mov_b32_e32 v74, v114
	v_mov_b32_e32 v75, v115
	v_mov_b32_e32 v76, v120
	v_mov_b32_e32 v77, v121
	v_mov_b32_e32 v78, v116
	v_mov_b32_e32 v79, v117
	v_mov_b32_e32 v80, v118
	v_mov_b32_e32 v81, v119
	v_mov_b32_e32 v90, v98
	v_mov_b32_e32 v91, v99
	v_mov_b32_e32 v92, v104
	v_mov_b32_e32 v93, v105
	v_mov_b32_e32 v94, v100
	v_mov_b32_e32 v95, v101
	v_mov_b32_e32 v96, v102
	v_mov_b32_e32 v97, v103
	v_mov_b32_e32 v98, v106
	v_mov_b32_e32 v99, v107
	v_mov_b32_e32 v100, v112
	v_mov_b32_e32 v101, v113
	v_mov_b32_e32 v102, v108
	v_mov_b32_e32 v103, v109
	v_mov_b32_e32 v104, v110
	v_mov_b32_e32 v105, v111
	v_mov_b32_e32 v114, v122
	v_mov_b32_e32 v115, v123
	v_mov_b32_e32 v116, v128
	v_mov_b32_e32 v117, v129
	v_mov_b32_e32 v118, v124
	v_mov_b32_e32 v119, v125
	v_mov_b32_e32 v120, v126
	v_mov_b32_e32 v121, v127
	v_mov_b32_e32 v130, v24
	v_mov_b32_e32 v131, v25
	v_mov_b32_e32 v132, v30
	v_mov_b32_e32 v133, v31
	v_mov_b32_e32 v134, v26
	v_mov_b32_e32 v135, v27
	v_mov_b32_e32 v136, v28
	v_mov_b32_e32 v137, v29
	v_mov_b32_e32 v146, v8
	v_mov_b32_e32 v147, v9
	v_mov_b32_e32 v148, v14
	v_mov_b32_e32 v149, v15
	v_mov_b32_e32 v150, v10
	v_mov_b32_e32 v151, v11
	v_mov_b32_e32 v152, v12
	v_mov_b32_e32 v153, v13
	v_mov_b32_e32 v106, v154
	v_mov_b32_e32 v107, v155
	v_mov_b32_e32 v108, v160
	v_mov_b32_e32 v109, v161
	v_mov_b32_e32 v110, v156
	v_mov_b32_e32 v111, v157
	v_mov_b32_e32 v112, v158
	v_mov_b32_e32 v113, v159
	v_mov_b32_e32 v122, v138
	v_mov_b32_e32 v123, v139
	v_mov_b32_e32 v124, v144
	v_mov_b32_e32 v125, v145
	v_mov_b32_e32 v126, v140
	v_mov_b32_e32 v127, v141
	v_mov_b32_e32 v128, v142
	v_mov_b32_e32 v129, v143
	v_mov_b32_e32 v138, v16
	v_mov_b32_e32 v139, v17
	v_mov_b32_e32 v140, v22
	v_mov_b32_e32 v141, v23
	v_mov_b32_e32 v142, v18
	v_mov_b32_e32 v143, v19
	v_mov_b32_e32 v144, v20
	v_mov_b32_e32 v145, v21
	v_mov_b32_e32 v154, v0
	v_mov_b32_e32 v155, v1
	v_mov_b32_e32 v156, v6
	v_mov_b32_e32 v157, v7
	v_mov_b32_e32 v158, v2
	v_mov_b32_e32 v159, v3
	v_mov_b32_e32 v160, v4
	v_mov_b32_e32 v161, v5
	.p2align 6

.LBB0_1854:
	s_ashr_i32 s15, s14, 31
	s_lshl_b64 s[16:17], s[14:15], 18
	s_add_u32 s16, s26, s16
	s_addc_u32 s17, s27, s17
	s_and_b64 s[18:19], s[40:41], exec
	s_cselect_b32 s15, s17, s21
	s_cselect_b32 s55, s16, s20
	s_ashr_i32 s13, s12, 31
	s_lshl_b64 s[18:19], s[12:13], 18
	s_add_u32 s18, s33, s18
	s_addc_u32 s19, s34, s19
	s_and_b64 s[24:25], s[40:41], exec
	s_cselect_b32 s13, s19, s23
	s_cselect_b32 s56, s18, s22
	s_add_u32 s20, s20, 0x20080
	s_addc_u32 s21, s21, 0
	s_add_u32 s57, s22, 0x100
	v_mov_b32_e32 v32, 0
	s_addc_u32 s58, s23, 0
	s_mov_b32 s59, -2
	v_mov_b32_e32 v33, v32
	v_mov_b32_e32 v34, v32
	v_mov_b32_e32 v35, v32
	v_mov_b32_e32 v36, v32
	v_mov_b32_e32 v37, v32
	v_mov_b32_e32 v38, v32
	v_mov_b32_e32 v39, v32
	v_mov_b32_e32 v48, v32
	v_mov_b32_e32 v49, v32
	v_mov_b32_e32 v50, v32
	v_mov_b32_e32 v51, v32
	v_mov_b32_e32 v52, v32
	v_mov_b32_e32 v53, v32
	v_mov_b32_e32 v54, v32
	v_mov_b32_e32 v55, v32
	v_mov_b32_e32 v66, v32
	v_mov_b32_e32 v67, v32
	v_mov_b32_e32 v68, v32
	v_mov_b32_e32 v69, v32
	v_mov_b32_e32 v70, v32
	v_mov_b32_e32 v71, v32
	v_mov_b32_e32 v72, v32
	v_mov_b32_e32 v73, v32
	v_mov_b32_e32 v82, v32
	v_mov_b32_e32 v83, v32
	v_mov_b32_e32 v84, v32
	v_mov_b32_e32 v85, v32
	v_mov_b32_e32 v86, v32
	v_mov_b32_e32 v87, v32
	v_mov_b32_e32 v88, v32
	v_mov_b32_e32 v89, v32
	v_mov_b32_e32 v40, v32
	v_mov_b32_e32 v41, v32
	v_mov_b32_e32 v42, v32
	v_mov_b32_e32 v43, v32
	v_mov_b32_e32 v44, v32
	v_mov_b32_e32 v45, v32
	v_mov_b32_e32 v46, v32
	v_mov_b32_e32 v47, v32
	v_mov_b32_e32 v56, v32
	v_mov_b32_e32 v57, v32
	v_mov_b32_e32 v58, v32
	v_mov_b32_e32 v59, v32
	v_mov_b32_e32 v60, v32
	v_mov_b32_e32 v61, v32
	v_mov_b32_e32 v62, v32
	v_mov_b32_e32 v63, v32
	v_mov_b32_e32 v74, v32
	v_mov_b32_e32 v75, v32
	v_mov_b32_e32 v76, v32
	v_mov_b32_e32 v77, v32
	v_mov_b32_e32 v78, v32
	v_mov_b32_e32 v79, v32
	v_mov_b32_e32 v80, v32
	v_mov_b32_e32 v81, v32
	v_mov_b32_e32 v90, v32
	v_mov_b32_e32 v91, v32
	v_mov_b32_e32 v92, v32
	v_mov_b32_e32 v93, v32
	v_mov_b32_e32 v94, v32
	v_mov_b32_e32 v95, v32
	v_mov_b32_e32 v96, v32
	v_mov_b32_e32 v97, v32
	v_mov_b32_e32 v98, v32
	v_mov_b32_e32 v99, v32
	v_mov_b32_e32 v100, v32
	v_mov_b32_e32 v101, v32
	v_mov_b32_e32 v102, v32
	v_mov_b32_e32 v103, v32
	v_mov_b32_e32 v104, v32
	v_mov_b32_e32 v105, v32
	v_mov_b32_e32 v114, v32
	v_mov_b32_e32 v115, v32
	v_mov_b32_e32 v116, v32
	v_mov_b32_e32 v117, v32
	v_mov_b32_e32 v118, v32
	v_mov_b32_e32 v119, v32
	v_mov_b32_e32 v120, v32
	v_mov_b32_e32 v121, v32
	v_mov_b32_e32 v130, v32
	v_mov_b32_e32 v131, v32
	v_mov_b32_e32 v132, v32
	v_mov_b32_e32 v133, v32
	v_mov_b32_e32 v134, v32
	v_mov_b32_e32 v135, v32
	v_mov_b32_e32 v136, v32
	v_mov_b32_e32 v137, v32
	v_mov_b32_e32 v146, v32
	v_mov_b32_e32 v147, v32
	v_mov_b32_e32 v148, v32
	v_mov_b32_e32 v149, v32
	v_mov_b32_e32 v150, v32
	v_mov_b32_e32 v151, v32
	v_mov_b32_e32 v152, v32
	v_mov_b32_e32 v153, v32
	v_mov_b32_e32 v106, v32
	v_mov_b32_e32 v107, v32
	v_mov_b32_e32 v108, v32
	v_mov_b32_e32 v109, v32
	v_mov_b32_e32 v110, v32
	v_mov_b32_e32 v111, v32
	v_mov_b32_e32 v112, v32
	v_mov_b32_e32 v113, v32
	v_mov_b32_e32 v122, v32
	v_mov_b32_e32 v123, v32
	v_mov_b32_e32 v124, v32
	v_mov_b32_e32 v125, v32
	v_mov_b32_e32 v126, v32
	v_mov_b32_e32 v127, v32
	v_mov_b32_e32 v128, v32
	v_mov_b32_e32 v129, v32
	v_mov_b32_e32 v138, v32
	v_mov_b32_e32 v139, v32
	v_mov_b32_e32 v140, v32
	v_mov_b32_e32 v141, v32
	v_mov_b32_e32 v142, v32
	v_mov_b32_e32 v143, v32
	v_mov_b32_e32 v144, v32
	v_mov_b32_e32 v145, v32
	v_mov_b32_e32 v154, v32
	v_mov_b32_e32 v155, v32
	v_mov_b32_e32 v156, v32
	v_mov_b32_e32 v157, v32
	v_mov_b32_e32 v158, v32
	v_mov_b32_e32 v159, v32
	v_mov_b32_e32 v160, v32
	v_mov_b32_e32 v161, v32
	.p2align 6

.LBB0_2323:
	s_ashr_i32 s11, s10, 31
	s_lshl_b64 s[16:17], s[10:11], 18
	s_add_u32 s16, s33, s16
	s_addc_u32 s17, s42, s17
	s_and_b64 s[18:19], s[14:15], exec
	s_cselect_b32 s11, s17, s23
	s_cselect_b32 s21, s16, s22
	s_ashr_i32 s13, s12, 31
	s_lshl_b64 s[18:19], s[12:13], 18
	s_add_u32 s18, s43, s18
	s_addc_u32 s19, s44, s19
	s_and_b64 s[40:41], s[14:15], exec
	s_cselect_b32 s13, s19, s25
	s_cselect_b32 s57, s18, s24
	s_add_u32 s22, s22, 0x20080
	s_addc_u32 s23, s23, 0
	s_add_u32 s58, s24, 0x100
	v_mov_b32_e32 v32, 0
	s_addc_u32 s59, s25, 0
	s_mov_b32 s60, -2
	v_mov_b32_e32 v33, v32
	v_mov_b32_e32 v34, v32
	v_mov_b32_e32 v35, v32
	v_mov_b32_e32 v40, v32
	v_mov_b32_e32 v41, v32
	v_mov_b32_e32 v42, v32
	v_mov_b32_e32 v43, v32
	v_mov_b32_e32 v48, v32
	v_mov_b32_e32 v49, v32
	v_mov_b32_e32 v50, v32
	v_mov_b32_e32 v51, v32
	v_mov_b32_e32 v56, v32
	v_mov_b32_e32 v57, v32
	v_mov_b32_e32 v58, v32
	v_mov_b32_e32 v59, v32
	v_mov_b32_e32 v66, v32
	v_mov_b32_e32 v67, v32
	v_mov_b32_e32 v68, v32
	v_mov_b32_e32 v69, v32
	v_mov_b32_e32 v74, v32
	v_mov_b32_e32 v75, v32
	v_mov_b32_e32 v76, v32
	v_mov_b32_e32 v77, v32
	v_mov_b32_e32 v82, v32
	v_mov_b32_e32 v83, v32
	v_mov_b32_e32 v84, v32
	v_mov_b32_e32 v85, v32
	v_mov_b32_e32 v90, v32
	v_mov_b32_e32 v91, v32
	v_mov_b32_e32 v92, v32
	v_mov_b32_e32 v93, v32
	v_mov_b32_e32 v36, v32
	v_mov_b32_e32 v37, v32
	v_mov_b32_e32 v38, v32
	v_mov_b32_e32 v39, v32
	v_mov_b32_e32 v44, v32
	v_mov_b32_e32 v45, v32
	v_mov_b32_e32 v46, v32
	v_mov_b32_e32 v47, v32
	v_mov_b32_e32 v52, v32
	v_mov_b32_e32 v53, v32
	v_mov_b32_e32 v54, v32
	v_mov_b32_e32 v55, v32
	v_mov_b32_e32 v60, v32
	v_mov_b32_e32 v61, v32
	v_mov_b32_e32 v62, v32
	v_mov_b32_e32 v63, v32
	v_mov_b32_e32 v70, v32
	v_mov_b32_e32 v71, v32
	v_mov_b32_e32 v72, v32
	v_mov_b32_e32 v73, v32
	v_mov_b32_e32 v78, v32
	v_mov_b32_e32 v79, v32
	v_mov_b32_e32 v80, v32
	v_mov_b32_e32 v81, v32
	v_mov_b32_e32 v86, v32
	v_mov_b32_e32 v87, v32
	v_mov_b32_e32 v88, v32
	v_mov_b32_e32 v89, v32
	v_mov_b32_e32 v94, v32
	v_mov_b32_e32 v95, v32
	v_mov_b32_e32 v96, v32
	v_mov_b32_e32 v97, v32
	v_mov_b32_e32 v98, v32
	v_mov_b32_e32 v99, v32
	v_mov_b32_e32 v100, v32
	v_mov_b32_e32 v101, v32
	v_mov_b32_e32 v106, v32
	v_mov_b32_e32 v107, v32
	v_mov_b32_e32 v108, v32
	v_mov_b32_e32 v109, v32
	v_mov_b32_e32 v114, v32
	v_mov_b32_e32 v115, v32
	v_mov_b32_e32 v116, v32
	v_mov_b32_e32 v117, v32
	v_mov_b32_e32 v122, v32
	v_mov_b32_e32 v123, v32
	v_mov_b32_e32 v124, v32
	v_mov_b32_e32 v125, v32
	v_mov_b32_e32 v130, v32
	v_mov_b32_e32 v131, v32
	v_mov_b32_e32 v132, v32
	v_mov_b32_e32 v133, v32
	v_mov_b32_e32 v138, v32
	v_mov_b32_e32 v139, v32
	v_mov_b32_e32 v140, v32
	v_mov_b32_e32 v141, v32
	v_mov_b32_e32 v146, v32
	v_mov_b32_e32 v147, v32
	v_mov_b32_e32 v148, v32
	v_mov_b32_e32 v149, v32
	v_mov_b32_e32 v154, v32
	v_mov_b32_e32 v155, v32
	v_mov_b32_e32 v156, v32
	v_mov_b32_e32 v157, v32
	v_mov_b32_e32 v102, v32
	v_mov_b32_e32 v103, v32
	v_mov_b32_e32 v104, v32
	v_mov_b32_e32 v105, v32
	v_mov_b32_e32 v110, v32
	v_mov_b32_e32 v111, v32
	v_mov_b32_e32 v112, v32
	v_mov_b32_e32 v113, v32
	v_mov_b32_e32 v118, v32
	v_mov_b32_e32 v119, v32
	v_mov_b32_e32 v120, v32
	v_mov_b32_e32 v121, v32
	v_mov_b32_e32 v126, v32
	v_mov_b32_e32 v127, v32
	v_mov_b32_e32 v128, v32
	v_mov_b32_e32 v129, v32
	v_mov_b32_e32 v134, v32
	v_mov_b32_e32 v135, v32
	v_mov_b32_e32 v136, v32
	v_mov_b32_e32 v137, v32
	v_mov_b32_e32 v142, v32
	v_mov_b32_e32 v143, v32
	v_mov_b32_e32 v144, v32
	v_mov_b32_e32 v145, v32
	v_mov_b32_e32 v150, v32
	v_mov_b32_e32 v151, v32
	v_mov_b32_e32 v152, v32
	v_mov_b32_e32 v153, v32
	v_mov_b32_e32 v158, v32
	v_mov_b32_e32 v159, v32
	v_mov_b32_e32 v160, v32
	v_mov_b32_e32 v161, v32
	.p2align 6

.LBB0_2346:
	s_ashr_i32 s15, s14, 31
	s_lshl_b64 s[16:17], s[14:15], 18
	s_add_u32 s16, s26, s16
	s_addc_u32 s17, s27, s17
	s_and_b64 s[18:19], s[38:39], exec
	s_cselect_b32 s15, s17, s21
	s_cselect_b32 s53, s16, s20
	s_ashr_i32 s13, s12, 31
	s_lshl_b64 s[18:19], s[12:13], 18
	s_add_u32 s18, s33, s18
	s_addc_u32 s19, s34, s19
	s_and_b64 s[24:25], s[38:39], exec
	s_cselect_b32 s13, s19, s23
	s_cselect_b32 s54, s18, s22
	s_add_u32 s20, s20, 0x20080
	s_addc_u32 s21, s21, 0
	s_add_u32 s55, s22, 0x100
	v_mov_b32_e32 v32, 0
	s_addc_u32 s56, s23, 0
	s_mov_b32 s57, -2
	v_mov_b32_e32 v33, v32
	v_mov_b32_e32 v34, v32
	v_mov_b32_e32 v35, v32
	v_mov_b32_e32 v36, v32
	v_mov_b32_e32 v37, v32
	v_mov_b32_e32 v38, v32
	v_mov_b32_e32 v39, v32
	v_mov_b32_e32 v48, v32
	v_mov_b32_e32 v49, v32
	v_mov_b32_e32 v50, v32
	v_mov_b32_e32 v51, v32
	v_mov_b32_e32 v52, v32
	v_mov_b32_e32 v53, v32
	v_mov_b32_e32 v54, v32
	v_mov_b32_e32 v55, v32
	v_mov_b32_e32 v66, v32
	v_mov_b32_e32 v67, v32
	v_mov_b32_e32 v68, v32
	v_mov_b32_e32 v69, v32
	v_mov_b32_e32 v70, v32
	v_mov_b32_e32 v71, v32
	v_mov_b32_e32 v72, v32
	v_mov_b32_e32 v73, v32
	v_mov_b32_e32 v82, v32
	v_mov_b32_e32 v83, v32
	v_mov_b32_e32 v84, v32
	v_mov_b32_e32 v85, v32
	v_mov_b32_e32 v86, v32
	v_mov_b32_e32 v87, v32
	v_mov_b32_e32 v88, v32
	v_mov_b32_e32 v89, v32
	v_mov_b32_e32 v40, v32
	v_mov_b32_e32 v41, v32
	v_mov_b32_e32 v42, v32
	v_mov_b32_e32 v43, v32
	v_mov_b32_e32 v44, v32
	v_mov_b32_e32 v45, v32
	v_mov_b32_e32 v46, v32
	v_mov_b32_e32 v47, v32
	v_mov_b32_e32 v56, v32
	v_mov_b32_e32 v57, v32
	v_mov_b32_e32 v58, v32
	v_mov_b32_e32 v59, v32
	v_mov_b32_e32 v60, v32
	v_mov_b32_e32 v61, v32
	v_mov_b32_e32 v62, v32
	v_mov_b32_e32 v63, v32
	v_mov_b32_e32 v74, v32
	v_mov_b32_e32 v75, v32
	v_mov_b32_e32 v76, v32
	v_mov_b32_e32 v77, v32
	v_mov_b32_e32 v78, v32
	v_mov_b32_e32 v79, v32
	v_mov_b32_e32 v80, v32
	v_mov_b32_e32 v81, v32
	v_mov_b32_e32 v90, v32
	v_mov_b32_e32 v91, v32
	v_mov_b32_e32 v92, v32
	v_mov_b32_e32 v93, v32
	v_mov_b32_e32 v94, v32
	v_mov_b32_e32 v95, v32
	v_mov_b32_e32 v96, v32
	v_mov_b32_e32 v97, v32
	v_mov_b32_e32 v98, v32
	v_mov_b32_e32 v99, v32
	v_mov_b32_e32 v100, v32
	v_mov_b32_e32 v101, v32
	v_mov_b32_e32 v102, v32
	v_mov_b32_e32 v103, v32
	v_mov_b32_e32 v104, v32
	v_mov_b32_e32 v105, v32
	v_mov_b32_e32 v114, v32
	v_mov_b32_e32 v115, v32
	v_mov_b32_e32 v116, v32
	v_mov_b32_e32 v117, v32
	v_mov_b32_e32 v118, v32
	v_mov_b32_e32 v119, v32
	v_mov_b32_e32 v120, v32
	v_mov_b32_e32 v121, v32
	v_mov_b32_e32 v130, v32
	v_mov_b32_e32 v131, v32
	v_mov_b32_e32 v132, v32
	v_mov_b32_e32 v133, v32
	v_mov_b32_e32 v134, v32
	v_mov_b32_e32 v135, v32
	v_mov_b32_e32 v136, v32
	v_mov_b32_e32 v137, v32
	v_mov_b32_e32 v146, v32
	v_mov_b32_e32 v147, v32
	v_mov_b32_e32 v148, v32
	v_mov_b32_e32 v149, v32
	v_mov_b32_e32 v150, v32
	v_mov_b32_e32 v151, v32
	v_mov_b32_e32 v152, v32
	v_mov_b32_e32 v153, v32
	v_mov_b32_e32 v106, v32
	v_mov_b32_e32 v107, v32
	v_mov_b32_e32 v108, v32
	v_mov_b32_e32 v109, v32
	v_mov_b32_e32 v110, v32
	v_mov_b32_e32 v111, v32
	v_mov_b32_e32 v112, v32
	v_mov_b32_e32 v113, v32
	v_mov_b32_e32 v122, v32
	v_mov_b32_e32 v123, v32
	v_mov_b32_e32 v124, v32
	v_mov_b32_e32 v125, v32
	v_mov_b32_e32 v126, v32
	v_mov_b32_e32 v127, v32
	v_mov_b32_e32 v128, v32
	v_mov_b32_e32 v129, v32
	v_mov_b32_e32 v138, v32
	v_mov_b32_e32 v139, v32
	v_mov_b32_e32 v140, v32
	v_mov_b32_e32 v141, v32
	v_mov_b32_e32 v142, v32
	v_mov_b32_e32 v143, v32
	v_mov_b32_e32 v144, v32
	v_mov_b32_e32 v145, v32
	v_mov_b32_e32 v154, v32
	v_mov_b32_e32 v155, v32
	v_mov_b32_e32 v156, v32
	v_mov_b32_e32 v157, v32
	v_mov_b32_e32 v158, v32
	v_mov_b32_e32 v159, v32
	v_mov_b32_e32 v160, v32
	v_mov_b32_e32 v161, v32
	.p2align 6

.LBB0_2424:
	s_ashr_i32 s13, s12, 31
	s_lshl_b64 s[18:19], s[12:13], 18
	s_add_u32 s18, s33, s18
	s_addc_u32 s19, s46, s19
	s_and_b64 s[20:21], s[16:17], exec
	s_cselect_b32 s13, s19, s41
	s_cselect_b32 s23, s18, s40
	s_ashr_i32 s15, s14, 31
	s_lshl_b64 s[20:21], s[14:15], 18
	s_add_u32 s20, s47, s20
	s_addc_u32 s21, s48, s21
	s_and_b64 s[44:45], s[16:17], exec
	s_cselect_b32 s15, s21, s43
	s_cselect_b32 s56, s20, s42
	s_add_u32 s40, s40, 0x20080
	s_addc_u32 s41, s41, 0
	s_add_u32 s57, s42, 0x100
	v_mov_b32_e32 v32, 0
	s_addc_u32 s58, s43, 0
	s_mov_b32 s59, -2
	v_mov_b32_e32 v33, v32
	v_mov_b32_e32 v34, v32
	v_mov_b32_e32 v35, v32
	v_mov_b32_e32 v36, v32
	v_mov_b32_e32 v37, v32
	v_mov_b32_e32 v38, v32
	v_mov_b32_e32 v39, v32
	v_mov_b32_e32 v48, v32
	v_mov_b32_e32 v49, v32
	v_mov_b32_e32 v50, v32
	v_mov_b32_e32 v51, v32
	v_mov_b32_e32 v52, v32
	v_mov_b32_e32 v53, v32
	v_mov_b32_e32 v54, v32
	v_mov_b32_e32 v55, v32
	v_mov_b32_e32 v66, v32
	v_mov_b32_e32 v67, v32
	v_mov_b32_e32 v68, v32
	v_mov_b32_e32 v69, v32
	v_mov_b32_e32 v70, v32
	v_mov_b32_e32 v71, v32
	v_mov_b32_e32 v72, v32
	v_mov_b32_e32 v73, v32
	v_mov_b32_e32 v82, v32
	v_mov_b32_e32 v83, v32
	v_mov_b32_e32 v84, v32
	v_mov_b32_e32 v85, v32
	v_mov_b32_e32 v86, v32
	v_mov_b32_e32 v87, v32
	v_mov_b32_e32 v88, v32
	v_mov_b32_e32 v89, v32
	v_mov_b32_e32 v40, v32
	v_mov_b32_e32 v41, v32
	v_mov_b32_e32 v42, v32
	v_mov_b32_e32 v43, v32
	v_mov_b32_e32 v44, v32
	v_mov_b32_e32 v45, v32
	v_mov_b32_e32 v46, v32
	v_mov_b32_e32 v47, v32
	v_mov_b32_e32 v56, v32
	v_mov_b32_e32 v57, v32
	v_mov_b32_e32 v58, v32
	v_mov_b32_e32 v59, v32
	v_mov_b32_e32 v60, v32
	v_mov_b32_e32 v61, v32
	v_mov_b32_e32 v62, v32
	v_mov_b32_e32 v63, v32
	v_mov_b32_e32 v74, v32
	v_mov_b32_e32 v75, v32
	v_mov_b32_e32 v76, v32
	v_mov_b32_e32 v77, v32
	v_mov_b32_e32 v78, v32
	v_mov_b32_e32 v79, v32
	v_mov_b32_e32 v80, v32
	v_mov_b32_e32 v81, v32
	v_mov_b32_e32 v90, v32
	v_mov_b32_e32 v91, v32
	v_mov_b32_e32 v92, v32
	v_mov_b32_e32 v93, v32
	v_mov_b32_e32 v94, v32
	v_mov_b32_e32 v95, v32
	v_mov_b32_e32 v96, v32
	v_mov_b32_e32 v97, v32
	v_mov_b32_e32 v98, v32
	v_mov_b32_e32 v99, v32
	v_mov_b32_e32 v100, v32
	v_mov_b32_e32 v101, v32
	v_mov_b32_e32 v102, v32
	v_mov_b32_e32 v103, v32
	v_mov_b32_e32 v104, v32
	v_mov_b32_e32 v105, v32
	v_mov_b32_e32 v114, v32
	v_mov_b32_e32 v115, v32
	v_mov_b32_e32 v116, v32
	v_mov_b32_e32 v117, v32
	v_mov_b32_e32 v118, v32
	v_mov_b32_e32 v119, v32
	v_mov_b32_e32 v120, v32
	v_mov_b32_e32 v121, v32
	v_mov_b32_e32 v130, v32
	v_mov_b32_e32 v131, v32
	v_mov_b32_e32 v132, v32
	v_mov_b32_e32 v133, v32
	v_mov_b32_e32 v134, v32
	v_mov_b32_e32 v135, v32
	v_mov_b32_e32 v136, v32
	v_mov_b32_e32 v137, v32
	v_mov_b32_e32 v146, v32
	v_mov_b32_e32 v147, v32
	v_mov_b32_e32 v148, v32
	v_mov_b32_e32 v149, v32
	v_mov_b32_e32 v150, v32
	v_mov_b32_e32 v151, v32
	v_mov_b32_e32 v152, v32
	v_mov_b32_e32 v153, v32
	v_mov_b32_e32 v106, v32
	v_mov_b32_e32 v107, v32
	v_mov_b32_e32 v108, v32
	v_mov_b32_e32 v109, v32
	v_mov_b32_e32 v110, v32
	v_mov_b32_e32 v111, v32
	v_mov_b32_e32 v112, v32
	v_mov_b32_e32 v113, v32
	v_mov_b32_e32 v122, v32
	v_mov_b32_e32 v123, v32
	v_mov_b32_e32 v124, v32
	v_mov_b32_e32 v125, v32
	v_mov_b32_e32 v126, v32
	v_mov_b32_e32 v127, v32
	v_mov_b32_e32 v128, v32
	v_mov_b32_e32 v129, v32
	v_mov_b32_e32 v138, v32
	v_mov_b32_e32 v139, v32
	v_mov_b32_e32 v140, v32
	v_mov_b32_e32 v141, v32
	v_mov_b32_e32 v142, v32
	v_mov_b32_e32 v143, v32
	v_mov_b32_e32 v144, v32
	v_mov_b32_e32 v145, v32
	v_mov_b32_e32 v154, v32
	v_mov_b32_e32 v155, v32
	v_mov_b32_e32 v156, v32
	v_mov_b32_e32 v157, v32
	v_mov_b32_e32 v158, v32
	v_mov_b32_e32 v159, v32
	v_mov_b32_e32 v160, v32
	v_mov_b32_e32 v161, v32
	.p2align 6
